# wconv rewritten by hand: 128x128 tiles, 16 loads in flight per lane, swizzled fp16 LDS image, tile-less blocks exit at once; plus 4-phase GEMM loops
# speedup vs baseline: 1.0170x; 1.0006x over previous
_Z12wconv_kernel5WDesci:
	s_movk_i32 s5, 0x400
	s_cmp_lt_u32 s3, 5
	s_cselect_b32 s4, 0x100, s5
	s_cmp_ge_u32 s2, s4
	s_cbranch_scc1 .Lwc_exit
	s_mov_b32 s4, s2
.Lwc_work:
	s_load_dword s8, s[0:1], 0x150
	s_cmp_eq_u32 s3, 5
	s_cselect_b32 s9, 13, 11
	s_cmp_eq_u32 s3, 6
	s_cselect_b32 s10, 13, 11
	s_sub_u32 s11, s9, 7
	s_lshr_b32 s12, s4, s11
	s_lshl_b32 s13, s12, s11
	s_sub_u32 s13, s4, s13
	s_add_u32 s20, s9, 2
	s_add_u32 s21, s10, 1
	v_lshrrev_b32_e32 v4, 5, v0
	v_and_b32_e32 v6, 31, v0
	v_lshlrev_b32_e32 v5, 4, v4
	v_lshlrev_b32_e32 v5, s20, v5
	v_lshl_add_u32 v1, v6, 4, v5
	v_lshlrev_b32_e32 v7, 1, v4
	v_and_b32_e32 v8, 7, v6
	v_xor_b32_e32 v7, v7, v8
	v_lshlrev_b32_e32 v7, 4, v7
	v_lshl_add_u32 v2, v6, 10, v7
	v_xor_b32_e32 v3, 16, v2
	v_lshrrev_b32_e32 v9, 4, v0
	v_and_b32_e32 v10, 15, v0
	v_lshrrev_b32_e32 v11, 6, v0
	v_xor_b32_e32 v11, v10, v11
	v_lshlrev_b32_e32 v11, 4, v11
	v_lshl_add_u32 v100, v9, 8, v11
	v_xor_b32_e32 v101, 64, v100
	v_lshlrev_b32_e32 v12, s21, v9
	v_lshl_add_u32 v102, v10, 4, v12
	s_add_u32 s22, s20, 7
	s_lshl_b32 s23, s12, s22
	s_lshl_b32 s24, s13, 9
	s_add_u32 s23, s23, s24
	s_lshl_b32 s25, 1, s20
	s_add_u32 s26, s21, 7
	s_lshl_b32 s27, s13, s26
	s_lshl_b32 s28, s12, 8
	s_add_u32 s27, s27, s28
	s_add_u32 s29, s10, 5
	s_lshl_b32 s29, 1, s29
	s_waitcnt lgkmcnt(0)
	s_add_u32 s8, s8, s3
	s_lshl_b32 s8, s8, 3
	s_add_u32 s14, s0, s8
	s_addc_u32 s15, s1, 0
	s_load_dwordx2 s[16:17], s[14:15], 0x0
	s_load_dwordx2 s[18:19], s[14:15], 0x70
	s_waitcnt lgkmcnt(0)
	s_add_u32 s16, s16, s23
	s_addc_u32 s17, s17, 0
	s_add_u32 s18, s18, s27
	s_addc_u32 s19, s19, 0
	global_load_dwordx4 v[4:7], v1, s[16:17] nt
	s_add_u32 s16, s16, s25
	s_addc_u32 s17, s17, 0
	global_load_dwordx4 v[8:11], v1, s[16:17] nt
	s_add_u32 s16, s16, s25
	s_addc_u32 s17, s17, 0
	global_load_dwordx4 v[12:15], v1, s[16:17] nt
	s_add_u32 s16, s16, s25
	s_addc_u32 s17, s17, 0
	global_load_dwordx4 v[16:19], v1, s[16:17] nt
	s_add_u32 s16, s16, s25
	s_addc_u32 s17, s17, 0
	global_load_dwordx4 v[20:23], v1, s[16:17] nt
	s_add_u32 s16, s16, s25
	s_addc_u32 s17, s17, 0
	global_load_dwordx4 v[24:27], v1, s[16:17] nt
	s_add_u32 s16, s16, s25
	s_addc_u32 s17, s17, 0
	global_load_dwordx4 v[28:31], v1, s[16:17] nt
	s_add_u32 s16, s16, s25
	s_addc_u32 s17, s17, 0
	global_load_dwordx4 v[32:35], v1, s[16:17] nt
	s_add_u32 s16, s16, s25
	s_addc_u32 s17, s17, 0
	global_load_dwordx4 v[36:39], v1, s[16:17] nt
	s_add_u32 s16, s16, s25
	s_addc_u32 s17, s17, 0
	global_load_dwordx4 v[40:43], v1, s[16:17] nt
	s_add_u32 s16, s16, s25
	s_addc_u32 s17, s17, 0
	global_load_dwordx4 v[44:47], v1, s[16:17] nt
	s_add_u32 s16, s16, s25
	s_addc_u32 s17, s17, 0
	global_load_dwordx4 v[48:51], v1, s[16:17] nt
	s_add_u32 s16, s16, s25
	s_addc_u32 s17, s17, 0
	global_load_dwordx4 v[52:55], v1, s[16:17] nt
	s_add_u32 s16, s16, s25
	s_addc_u32 s17, s17, 0
	global_load_dwordx4 v[56:59], v1, s[16:17] nt
	s_add_u32 s16, s16, s25
	s_addc_u32 s17, s17, 0
	global_load_dwordx4 v[60:63], v1, s[16:17] nt
	s_add_u32 s16, s16, s25
	s_addc_u32 s17, s17, 0
	global_load_dwordx4 v[64:67], v1, s[16:17] nt
	s_waitcnt vmcnt(14)
	v_cvt_pk_f16_f32 v68, v4, v8
	v_cvt_pk_f16_f32 v76, v5, v9
	v_cvt_pk_f16_f32 v84, v6, v10
	v_cvt_pk_f16_f32 v92, v7, v11
	s_waitcnt vmcnt(12)
	v_cvt_pk_f16_f32 v69, v12, v16
	v_cvt_pk_f16_f32 v77, v13, v17
	v_cvt_pk_f16_f32 v85, v14, v18
	v_cvt_pk_f16_f32 v93, v15, v19
	s_waitcnt vmcnt(10)
	v_cvt_pk_f16_f32 v70, v20, v24
	v_cvt_pk_f16_f32 v78, v21, v25
	v_cvt_pk_f16_f32 v86, v22, v26
	v_cvt_pk_f16_f32 v94, v23, v27
	s_waitcnt vmcnt(8)
	v_cvt_pk_f16_f32 v71, v28, v32
	v_cvt_pk_f16_f32 v79, v29, v33
	v_cvt_pk_f16_f32 v87, v30, v34
	v_cvt_pk_f16_f32 v95, v31, v35
	ds_write_b128 v2, v[68:71]
	ds_write_b128 v2, v[76:79] offset:256
	ds_write_b128 v2, v[84:87] offset:512
	ds_write_b128 v2, v[92:95] offset:768
	s_waitcnt vmcnt(6)
	v_cvt_pk_f16_f32 v72, v36, v40
	v_cvt_pk_f16_f32 v80, v37, v41
	v_cvt_pk_f16_f32 v88, v38, v42
	v_cvt_pk_f16_f32 v96, v39, v43
	s_waitcnt vmcnt(4)
	v_cvt_pk_f16_f32 v73, v44, v48
	v_cvt_pk_f16_f32 v81, v45, v49
	v_cvt_pk_f16_f32 v89, v46, v50
	v_cvt_pk_f16_f32 v97, v47, v51
	s_waitcnt vmcnt(2)
	v_cvt_pk_f16_f32 v74, v52, v56
	v_cvt_pk_f16_f32 v82, v53, v57
	v_cvt_pk_f16_f32 v90, v54, v58
	v_cvt_pk_f16_f32 v98, v55, v59
	s_waitcnt vmcnt(0)
	v_cvt_pk_f16_f32 v75, v60, v64
	v_cvt_pk_f16_f32 v83, v61, v65
	v_cvt_pk_f16_f32 v91, v62, v66
	v_cvt_pk_f16_f32 v99, v63, v67
	ds_write_b128 v3, v[72:75]
	ds_write_b128 v3, v[80:83] offset:256
	ds_write_b128 v3, v[88:91] offset:512
	ds_write_b128 v3, v[96:99] offset:768
	s_waitcnt lgkmcnt(0)
	s_barrier
	ds_read_b128 v[4:7], v100
	ds_read_b128 v[8:11], v101 offset:4096
	ds_read_b128 v[12:15], v100 offset:8192
	ds_read_b128 v[16:19], v101 offset:12288
	ds_read_b128 v[20:23], v100 offset:16384
	ds_read_b128 v[24:27], v101 offset:20480
	ds_read_b128 v[28:31], v100 offset:24576
	ds_read_b128 v[32:35], v101 offset:28672
	s_waitcnt lgkmcnt(7)
	global_store_dwordx4 v102, v[4:7], s[18:19]
	s_add_u32 s18, s18, s29
	s_addc_u32 s19, s19, 0
	s_waitcnt lgkmcnt(6)
	global_store_dwordx4 v102, v[8:11], s[18:19]
	s_add_u32 s18, s18, s29
	s_addc_u32 s19, s19, 0
	s_waitcnt lgkmcnt(5)
	global_store_dwordx4 v102, v[12:15], s[18:19]
	s_add_u32 s18, s18, s29
	s_addc_u32 s19, s19, 0
	s_waitcnt lgkmcnt(4)
	global_store_dwordx4 v102, v[16:19], s[18:19]
	s_add_u32 s18, s18, s29
	s_addc_u32 s19, s19, 0
	s_waitcnt lgkmcnt(3)
	global_store_dwordx4 v102, v[20:23], s[18:19]
	s_add_u32 s18, s18, s29
	s_addc_u32 s19, s19, 0
	s_waitcnt lgkmcnt(2)
	global_store_dwordx4 v102, v[24:27], s[18:19]
	s_add_u32 s18, s18, s29
	s_addc_u32 s19, s19, 0
	s_waitcnt lgkmcnt(1)
	global_store_dwordx4 v102, v[28:31], s[18:19]
	s_add_u32 s18, s18, s29
	s_addc_u32 s19, s19, 0
	s_waitcnt lgkmcnt(0)
	global_store_dwordx4 v102, v[32:35], s[18:19]

	.amdhsa_kernel _Z12wconv_kernel5WDesci
		.amdhsa_group_segment_fixed_size 32768
		.amdhsa_private_segment_fixed_size 0
		.amdhsa_kernarg_size 340
		.amdhsa_user_sgpr_count 2
		.amdhsa_user_sgpr_dispatch_ptr 0
		.amdhsa_user_sgpr_queue_ptr 0
		.amdhsa_user_sgpr_kernarg_segment_ptr 1
		.amdhsa_user_sgpr_dispatch_id 0
		.amdhsa_user_sgpr_kernarg_preload_length 0
		.amdhsa_user_sgpr_kernarg_preload_offset 0
		.amdhsa_user_sgpr_private_segment_size 0
		.amdhsa_uses_dynamic_stack 0
		.amdhsa_enable_private_segment 0
		.amdhsa_system_sgpr_workgroup_id_x 1
		.amdhsa_system_sgpr_workgroup_id_y 1
		.amdhsa_system_sgpr_workgroup_id_z 0
		.amdhsa_system_sgpr_workgroup_info 0
		.amdhsa_system_vgpr_workitem_id 0
		.amdhsa_next_free_vgpr 103
		.amdhsa_next_free_sgpr 30
		.amdhsa_accum_offset 104
		.amdhsa_reserve_vcc 0
		.amdhsa_float_round_mode_32 0
		.amdhsa_float_round_mode_16_64 0
		.amdhsa_float_denorm_mode_32 3
		.amdhsa_float_denorm_mode_16_64 3
		.amdhsa_dx10_clamp 1
		.amdhsa_ieee_mode 1
		.amdhsa_fp16_overflow 0
		.amdhsa_tg_split 0
		.amdhsa_exception_fp_ieee_invalid_op 0
		.amdhsa_exception_fp_denorm_src 0
		.amdhsa_exception_fp_ieee_div_zero 0
		.amdhsa_exception_fp_ieee_overflow 0
		.amdhsa_exception_fp_ieee_underflow 0
		.amdhsa_exception_fp_ieee_inexact 0
		.amdhsa_exception_int_div_zero 0
	.end_amdhsa_kernel

amdhsa.kernels:
  - .agpr_count:     0
    .args:
      - .offset:         0
        .size:           336
        .value_kind:     by_value
      - .offset:         336
        .size:           4
        .value_kind:     by_value
    .group_segment_fixed_size: 32768
    .kernarg_segment_align: 8
    .kernarg_segment_size: 340
    .language:       OpenCL C
    .language_version:
      - 2
      - 0
    .max_flat_workgroup_size: 256
    .name:           _Z12wconv_kernel5WDesci
    .private_segment_fixed_size: 0
    .sgpr_count:     36
    .sgpr_spill_count: 0
    .symbol:         _Z12wconv_kernel5WDesci.kd
    .uniform_work_group_size: 1
    .uses_dynamic_stack: false
    .vgpr_count:     103
    .vgpr_spill_count: 0
    .wavefront_size: 64
  - .agpr_count:     160
    .args:
      - .actual_access:  read_only
        .address_space:  global
        .offset:         0
        .size:           8
        .value_kind:     global_buffer
      - .address_space:  global
        .offset:         8
        .size:           8
        .value_kind:     global_buffer
      - .address_space:  global
        .offset:         16
        .size:           8
        .value_kind:     global_buffer
      - .actual_access:  read_only
        .address_space:  global
        .offset:         24
        .size:           8
        .value_kind:     global_buffer
      - .actual_access:  read_only
        .address_space:  global
        .offset:         32
        .size:           8
        .value_kind:     global_buffer
      - .actual_access:  read_only
        .address_space:  global
        .offset:         40
        .size:           8
        .value_kind:     global_buffer
      - .actual_access:  write_only
        .address_space:  global
        .offset:         48
        .size:           8
        .value_kind:     global_buffer
    .group_segment_fixed_size: 0
    .kernarg_segment_align: 8
    .kernarg_segment_size: 56
    .language:       OpenCL C
    .language_version:
      - 2
      - 0
    .max_flat_workgroup_size: 256
    .name:           _Z8ret_fastPKtS0_S0_S0_PKfS2_Pt
    .private_segment_fixed_size: 0
    .sgpr_count:     85
    .sgpr_spill_count: 0
    .symbol:         _Z8ret_fastPKtS0_S0_S0_PKfS2_Pt.kd
    .uniform_work_group_size: 1
    .uses_dynamic_stack: false
    .vgpr_count:     348
    .vgpr_spill_count: 0
    .wavefront_size: 64
  - .agpr_count:     0
    .args:
      - .actual_access:  read_only
        .address_space:  global
        .offset:         0
        .size:           8
        .value_kind:     global_buffer
      - .actual_access:  read_only
        .address_space:  global
        .offset:         8
        .size:           8
        .value_kind:     global_buffer
      - .actual_access:  read_only
        .address_space:  global
        .offset:         16
        .size:           8
        .value_kind:     global_buffer
      - .actual_access:  read_only
        .address_space:  global
        .offset:         24
        .size:           8
        .value_kind:     global_buffer
      - .actual_access:  write_only
        .address_space:  global
        .offset:         32
        .size:           8
        .value_kind:     global_buffer
      - .actual_access:  write_only
        .address_space:  global
        .offset:         40
        .size:           8
        .value_kind:     global_buffer
      - .actual_access:  read_only
        .address_space:  global
        .offset:         48
        .size:           8
        .value_kind:     global_buffer
      - .actual_access:  read_only
        .address_space:  global
        .offset:         56
        .size:           8
        .value_kind:     global_buffer
    .group_segment_fixed_size: 16
    .kernarg_segment_align: 8
    .kernarg_segment_size: 64
    .language:       OpenCL C
    .language_version:
      - 2
      - 0
    .max_flat_workgroup_size: 256
    .name:           _Z9ln_kernelILb0ELb0EEvPKvPKtS3_PKfPvPtS5_S5_
    .private_segment_fixed_size: 0
    .sgpr_count:     28
    .sgpr_spill_count: 0
    .symbol:         _Z9ln_kernelILb0ELb0EEvPKvPKtS3_PKfPvPtS5_S5_.kd
    .uniform_work_group_size: 1
    .uses_dynamic_stack: false
    .vgpr_count:     32
    .vgpr_spill_count: 0
    .wavefront_size: 64
  - .agpr_count:     0
    .args:
      - .actual_access:  read_only
        .address_space:  global
        .offset:         0
        .size:           8
        .value_kind:     global_buffer
      - .actual_access:  read_only
        .address_space:  global
        .offset:         8
        .size:           8
        .value_kind:     global_buffer
      - .actual_access:  read_only
        .address_space:  global
        .offset:         16
        .size:           8
        .value_kind:     global_buffer
      - .actual_access:  read_only
        .address_space:  global
        .offset:         24
        .size:           8
        .value_kind:     global_buffer
      - .actual_access:  write_only
        .address_space:  global
        .offset:         32
        .size:           8
        .value_kind:     global_buffer
      - .actual_access:  write_only
        .address_space:  global
        .offset:         40
        .size:           8
        .value_kind:     global_buffer
      - .actual_access:  read_only
        .address_space:  global
        .offset:         48
        .size:           8
        .value_kind:     global_buffer
      - .actual_access:  read_only
        .address_space:  global
        .offset:         56
        .size:           8
        .value_kind:     global_buffer
    .group_segment_fixed_size: 16
    .kernarg_segment_align: 8
    .kernarg_segment_size: 64
    .language:       OpenCL C
    .language_version:
      - 2
      - 0
    .max_flat_workgroup_size: 256
    .name:           _Z9ln_kernelILb1ELb1EEvPKvPKtS3_PKfPvPtS5_S5_
    .private_segment_fixed_size: 0
    .sgpr_count:     24
    .sgpr_spill_count: 0
    .symbol:         _Z9ln_kernelILb1ELb1EEvPKvPKtS3_PKfPvPtS5_S5_.kd
    .uniform_work_group_size: 1
    .uses_dynamic_stack: false
    .vgpr_count:     32
    .vgpr_spill_count: 0
    .wavefront_size: 64
  - .agpr_count:     0
    .args:
      - .address_space:  global
        .offset:         0
        .size:           8
        .value_kind:     global_buffer
      - .address_space:  global
        .offset:         8
        .size:           8
        .value_kind:     global_buffer
      - .offset:         16
        .size:           4
        .value_kind:     by_value
      - .offset:         20
        .size:           4
        .value_kind:     by_value
      - .offset:         24
        .size:           4
        .value_kind:     by_value
      - .offset:         28
        .size:           4
        .value_kind:     by_value
      - .offset:         32
        .size:           40
        .value_kind:     by_value
      - .offset:         72
        .size:           4
        .value_kind:     hidden_block_count_x
      - .offset:         76
        .size:           4
        .value_kind:     hidden_block_count_y
      - .offset:         80
        .size:           4
        .value_kind:     hidden_block_count_z
      - .offset:         84
        .size:           2
        .value_kind:     hidden_group_size_x
      - .offset:         86
        .size:           2
        .value_kind:     hidden_group_size_y
      - .offset:         88
        .size:           2
        .value_kind:     hidden_group_size_z
      - .offset:         90
        .size:           2
        .value_kind:     hidden_remainder_x
      - .offset:         92
        .size:           2
        .value_kind:     hidden_remainder_y
      - .offset:         94
        .size:           2
        .value_kind:     hidden_remainder_z
      - .offset:         112
        .size:           8
        .value_kind:     hidden_global_offset_x
      - .offset:         120
        .size:           8
        .value_kind:     hidden_global_offset_y
      - .offset:         128
        .size:           8
        .value_kind:     hidden_global_offset_z
      - .offset:         136
        .size:           2
        .value_kind:     hidden_grid_dims
      - .offset:         192
        .size:           4
        .value_kind:     hidden_dynamic_lds_size
    .group_segment_fixed_size: 0
    .kernarg_segment_align: 8
    .kernarg_segment_size: 328
    .language:       OpenCL C
    .language_version:
      - 2
      - 0
    .max_flat_workgroup_size: 512
    .name:           _Z9gemm_fastILi0ELi2EEvPKtS1_iiii7EpiArgs
    .private_segment_fixed_size: 0
    .sgpr_count:     55
    .sgpr_spill_count: 0
    .symbol:         _Z9gemm_fastILi0ELi2EEvPKtS1_iiii7EpiArgs.kd
    .uniform_work_group_size: 1
    .uses_dynamic_stack: false
    .vgpr_count:     255
    .vgpr_spill_count: 0
    .wavefront_size: 64
  - .agpr_count:     0
    .args:
      - .address_space:  global
        .offset:         0
        .size:           8
        .value_kind:     global_buffer
      - .address_space:  global
        .offset:         8
        .size:           8
        .value_kind:     global_buffer
      - .offset:         16
        .size:           4
        .value_kind:     by_value
      - .offset:         20
        .size:           4
        .value_kind:     by_value
      - .offset:         24
        .size:           4
        .value_kind:     by_value
      - .offset:         28
        .size:           4
        .value_kind:     by_value
      - .offset:         32
        .size:           40
        .value_kind:     by_value
    .group_segment_fixed_size: 0
    .kernarg_segment_align: 8
    .kernarg_segment_size: 72
    .language:       OpenCL C
    .language_version:
      - 2
      - 0
    .max_flat_workgroup_size: 512
    .name:           _Z9gemm_fastILi1ELi1EEvPKtS1_iiii7EpiArgs
    .private_segment_fixed_size: 0
    .sgpr_count:     32
    .sgpr_spill_count: 0
    .symbol:         _Z9gemm_fastILi1ELi1EEvPKtS1_iiii7EpiArgs.kd
    .uniform_work_group_size: 1
    .uses_dynamic_stack: false
    .vgpr_count:     247
    .vgpr_spill_count: 0
    .wavefront_size: 64
  - .agpr_count:     0
    .args:
      - .actual_access:  read_only
        .address_space:  global
        .offset:         0
        .size:           8
        .value_kind:     global_buffer
      - .actual_access:  read_only
        .address_space:  global
        .offset:         8
        .size:           8
        .value_kind:     global_buffer
      - .actual_access:  read_only
        .address_space:  global
        .offset:         16
        .size:           8
        .value_kind:     global_buffer
      - .actual_access:  read_only
        .address_space:  global
        .offset:         24
        .size:           8
        .value_kind:     global_buffer
      - .actual_access:  write_only
        .address_space:  global
        .offset:         32
        .size:           8
        .value_kind:     global_buffer
      - .actual_access:  write_only
        .address_space:  global
        .offset:         40
        .size:           8
        .value_kind:     global_buffer
      - .actual_access:  read_only
        .address_space:  global
        .offset:         48
        .size:           8
        .value_kind:     global_buffer
      - .actual_access:  read_only
        .address_space:  global
        .offset:         56
        .size:           8
        .value_kind:     global_buffer
    .group_segment_fixed_size: 16
    .kernarg_segment_align: 8
    .kernarg_segment_size: 64
    .language:       OpenCL C
    .language_version:
      - 2
      - 0
    .max_flat_workgroup_size: 256
    .name:           _Z9ln_kernelILb0ELb1EEvPKvPKtS3_PKfPvPtS5_S5_
    .private_segment_fixed_size: 0
    .sgpr_count:     28
    .sgpr_spill_count: 0
    .symbol:         _Z9ln_kernelILb0ELb1EEvPKvPKtS3_PKfPvPtS5_S5_.kd
    .uniform_work_group_size: 1
    .uses_dynamic_stack: false
    .vgpr_count:     30
    .vgpr_spill_count: 0
    .wavefront_size: 64
  - .agpr_count:     0
    .args:
      - .address_space:  global
        .offset:         0
        .size:           8
        .value_kind:     global_buffer
      - .address_space:  global
        .offset:         8
        .size:           8
        .value_kind:     global_buffer
      - .offset:         16
        .size:           4
        .value_kind:     by_value
      - .offset:         20
        .size:           4
        .value_kind:     by_value
      - .offset:         24
        .size:           4
        .value_kind:     by_value
      - .offset:         28
        .size:           4
        .value_kind:     by_value
      - .offset:         32
        .size:           40
        .value_kind:     by_value
      - .offset:         72
        .size:           4
        .value_kind:     hidden_block_count_x
      - .offset:         76
        .size:           4
        .value_kind:     hidden_block_count_y
      - .offset:         80
        .size:           4
        .value_kind:     hidden_block_count_z
      - .offset:         84
        .size:           2
        .value_kind:     hidden_group_size_x
      - .offset:         86
        .size:           2
        .value_kind:     hidden_group_size_y
      - .offset:         88
        .size:           2
        .value_kind:     hidden_group_size_z
      - .offset:         90
        .size:           2
        .value_kind:     hidden_remainder_x
      - .offset:         92
        .size:           2
        .value_kind:     hidden_remainder_y
      - .offset:         94
        .size:           2
        .value_kind:     hidden_remainder_z
      - .offset:         112
        .size:           8
        .value_kind:     hidden_global_offset_x
      - .offset:         120
        .size:           8
        .value_kind:     hidden_global_offset_y
      - .offset:         128
        .size:           8
        .value_kind:     hidden_global_offset_z
      - .offset:         136
        .size:           2
        .value_kind:     hidden_grid_dims
      - .offset:         192
        .size:           4
        .value_kind:     hidden_dynamic_lds_size
    .group_segment_fixed_size: 0
    .kernarg_segment_align: 8
    .kernarg_segment_size: 328
    .language:       OpenCL C
    .language_version:
      - 2
      - 0
    .max_flat_workgroup_size: 512
    .name:           _Z9gemm_fastILi2ELi2EEvPKtS1_iiii7EpiArgs
    .private_segment_fixed_size: 0
    .sgpr_count:     53
    .sgpr_spill_count: 0
    .symbol:         _Z9gemm_fastILi2ELi2EEvPKtS1_iiii7EpiArgs.kd
    .uniform_work_group_size: 1
    .uses_dynamic_stack: false
    .vgpr_count:     248
    .vgpr_spill_count: 0
    .wavefront_size: 64
  - .agpr_count:     0
    .args:
      - .actual_access:  read_only
        .address_space:  global
        .offset:         0
        .size:           8
        .value_kind:     global_buffer
      - .actual_access:  read_only
        .address_space:  global
        .offset:         8
        .size:           8
        .value_kind:     global_buffer
      - .actual_access:  read_only
        .address_space:  global
        .offset:         16
        .size:           8
        .value_kind:     global_buffer
      - .actual_access:  read_only
        .address_space:  global
        .offset:         24
        .size:           8
        .value_kind:     global_buffer
      - .actual_access:  write_only
        .address_space:  global
        .offset:         32
        .size:           8
        .value_kind:     global_buffer
      - .actual_access:  write_only
        .address_space:  global
        .offset:         40
        .size:           8
        .value_kind:     global_buffer
      - .actual_access:  read_only
        .address_space:  global
        .offset:         48
        .size:           8
        .value_kind:     global_buffer
      - .actual_access:  read_only
        .address_space:  global
        .offset:         56
        .size:           8
        .value_kind:     global_buffer
    .group_segment_fixed_size: 16
    .kernarg_segment_align: 8
    .kernarg_segment_size: 64
    .language:       OpenCL C
    .language_version:
      - 2
      - 0
    .max_flat_workgroup_size: 256
    .name:           _Z9ln_kernelILb1ELb0EEvPKvPKtS3_PKfPvPtS5_S5_
    .private_segment_fixed_size: 0
    .sgpr_count:     26
    .sgpr_spill_count: 0
    .symbol:         _Z9ln_kernelILb1ELb0EEvPKvPKtS3_PKfPvPtS5_S5_.kd
    .uniform_work_group_size: 1
    .uses_dynamic_stack: false
    .vgpr_count:     32
    .vgpr_spill_count: 0
    .wavefront_size: 64
